# combo4 + strategy 10: P0 w_pq x sub-key fold (f32 GEMM) moved from packed-f32 VALU to v_mfma_f32_16x16x4_f32 (f32 operands, f32 accumulate), b128 LDS fragment reads
# speedup vs baseline: 1.0100x; 1.0100x over previous
.LBB0_52:
	s_lshl_b32 s2, s1, 6
	s_and_b32 s2, s2, 0xfc0
	s_lshl_b32 s3, s1, 1
	s_and_b32 s6, s3, 0xffffff80
	v_add_u32_e32 v0, s2, v14
	s_ashr_i32 s7, s6, 31
	v_ashrrev_i32_e32 v1, 31, v0
	v_lshl_add_u64 v[38:39], s[6:7], 2, v[10:11]
	v_lshlrev_b64 v[0:1], 13, v[0:1]
	v_lshl_add_u64 v[40:41], v[38:39], 0, v[0:1]
	v_add_u32_e32 v0, s2, v16
	v_ashrrev_i32_e32 v1, 31, v0
	v_lshlrev_b64 v[0:1], 13, v[0:1]
	v_lshl_add_u64 v[42:43], v[38:39], 0, v[0:1]
	global_load_dwordx4 v[0:3], v[40:41], off
	global_load_dwordx4 v[4:7], v[42:43], off
	v_add_u32_e32 v40, s2, v18
	v_add_u32_e32 v42, s2, v20
	s_and_b32 s3, s1, 64
	v_ashrrev_i32_e32 v41, 31, v40
	v_ashrrev_i32_e32 v43, 31, v42
	s_cmp_eq_u32 s3, 0
	v_lshlrev_b64 v[40:41], 13, v[40:41]
	v_lshlrev_b64 v[42:43], 13, v[42:43]
	v_lshl_add_u64 v[40:41], v[38:39], 0, v[40:41]
	s_cselect_b32 s9, s15, s17
	s_cselect_b32 s8, s14, s16
	v_lshl_add_u64 v[38:39], v[38:39], 0, v[42:43]
	global_load_dwordx4 v[68:71], v[40:41], off
	global_load_dwordx4 v[72:75], v[38:39], off
	v_lshl_add_u64 v[38:39], s[8:9], 0, v[8:9]
	v_lshl_add_u64 v[40:41], v[38:39], 0, v[22:23]
	v_lshl_add_u64 v[44:45], v[38:39], 0, v[26:27]
	v_lshl_add_u64 v[42:43], v[38:39], 0, v[24:25]
	v_lshl_add_u64 v[46:47], v[38:39], 0, v[28:29]
	v_lshl_add_u64 v[48:49], v[38:39], 0, v[30:31]
	v_lshl_add_u64 v[50:51], v[38:39], 0, v[32:33]
	v_lshl_add_u64 v[52:53], v[38:39], 0, v[34:35]
	global_load_dwordx4 v[76:79], v[40:41], off
	global_load_dwordx4 v[80:83], v[42:43], off
	v_lshl_add_u64 v[38:39], v[38:39], 0, v[36:37]
	global_load_dwordx4 v[84:87], v[44:45], off
	global_load_dwordx4 v[88:91], v[46:47], off
	global_load_dwordx4 v[92:95], v[48:49], off
	global_load_dwordx4 v[96:99], v[50:51], off
	global_load_dwordx4 v[100:103], v[52:53], off
	global_load_dwordx4 v[104:107], v[38:39], off
	s_waitcnt vmcnt(11)
	ds_write_b128 v55, v[0:3]
	s_waitcnt vmcnt(10)
	ds_write_b128 v56, v[4:7]
	s_waitcnt vmcnt(9)
	ds_write_b128 v57, v[68:71]
	s_waitcnt vmcnt(8)
	ds_write_b128 v58, v[72:75]
	s_waitcnt vmcnt(7)
	ds_write_b128 v55, v[76:79] offset:33792
	s_waitcnt vmcnt(6)
	ds_write_b128 v56, v[80:83] offset:33792
	s_waitcnt vmcnt(5)
	ds_write_b128 v57, v[84:87] offset:33792
	s_waitcnt vmcnt(4)
	ds_write_b128 v58, v[88:91] offset:33792
	s_waitcnt vmcnt(3)
	ds_write_b128 v59, v[92:95] offset:33792
	s_waitcnt vmcnt(2)
	ds_write_b128 v60, v[96:99] offset:33792
	s_waitcnt vmcnt(1)
	ds_write_b128 v61, v[100:103] offset:33792
	s_waitcnt vmcnt(0)
	ds_write_b128 v62, v[104:107] offset:33792
	s_waitcnt lgkmcnt(0)
	s_barrier
	v_mbcnt_lo_u32_b32 v67, -1, 0
	v_mbcnt_hi_u32_b32 v67, -1, v67
	v_readlane_b32 s3, v254, 4
	v_and_b32_e32 v68, 15, v67
	v_lshrrev_b32_e32 v69, 4, v67
	s_lshr_b32 s3, s3, 2
	v_add_u32_e32 v70, s3, v68
	v_mul_u32_u24_e32 v71, 0x210, v68
	v_lshl_add_u32 v71, v69, 4, v71
	v_mul_u32_u24_e32 v72, 0x210, v70
	v_lshl_add_u32 v72, v69, 4, v72
	v_add_u32_e32 v72, 0x8400, v72
	v_mul_u32_u24_e32 v73, 0x90, v70
	v_lshl_add_u32 v73, v69, 3, v73
	v_mov_b32_e32 v74, 0
	v_mov_b32_e32 v75, 0
	v_mov_b32_e32 v76, 0
	v_mov_b32_e32 v77, 0
	v_mov_b32_e32 v78, 0
	v_mov_b32_e32 v79, 0
	v_mov_b32_e32 v80, 0
	v_mov_b32_e32 v81, 0
	v_mov_b32_e32 v82, 0
	v_mov_b32_e32 v83, 0
	v_mov_b32_e32 v84, 0
	v_mov_b32_e32 v85, 0
	v_mov_b32_e32 v86, 0
	v_mov_b32_e32 v87, 0
	v_mov_b32_e32 v88, 0
	v_mov_b32_e32 v89, 0
	ds_read_b128 v[90:93], v71
	ds_read_b128 v[94:97], v71 offset:8448
	ds_read_b128 v[98:101], v71 offset:16896
	ds_read_b128 v[102:105], v71 offset:25344
	ds_read_b128 v[106:109], v72
	ds_read_b128 v[110:113], v71 offset:64
	ds_read_b128 v[114:117], v71 offset:8512
	ds_read_b128 v[118:121], v71 offset:16960
	ds_read_b128 v[122:125], v71 offset:25408
	ds_read_b128 v[126:129], v72 offset:64
	s_waitcnt lgkmcnt(5)
	v_mfma_f32_16x16x4_f32 v[74:77], v90, v106, v[74:77]
	v_mfma_f32_16x16x4_f32 v[78:81], v94, v106, v[78:81]
	v_mfma_f32_16x16x4_f32 v[82:85], v98, v106, v[82:85]
	v_mfma_f32_16x16x4_f32 v[86:89], v102, v106, v[86:89]
	v_mfma_f32_16x16x4_f32 v[74:77], v91, v107, v[74:77]
	v_mfma_f32_16x16x4_f32 v[78:81], v95, v107, v[78:81]
	v_mfma_f32_16x16x4_f32 v[82:85], v99, v107, v[82:85]
	v_mfma_f32_16x16x4_f32 v[86:89], v103, v107, v[86:89]
	v_mfma_f32_16x16x4_f32 v[74:77], v92, v108, v[74:77]
	v_mfma_f32_16x16x4_f32 v[78:81], v96, v108, v[78:81]
	v_mfma_f32_16x16x4_f32 v[82:85], v100, v108, v[82:85]
	v_mfma_f32_16x16x4_f32 v[86:89], v104, v108, v[86:89]
	v_mfma_f32_16x16x4_f32 v[74:77], v93, v109, v[74:77]
	v_mfma_f32_16x16x4_f32 v[78:81], v97, v109, v[78:81]
	v_mfma_f32_16x16x4_f32 v[82:85], v101, v109, v[82:85]
	v_mfma_f32_16x16x4_f32 v[86:89], v105, v109, v[86:89]
	ds_read_b128 v[90:93], v71 offset:128
	ds_read_b128 v[94:97], v71 offset:8576
	ds_read_b128 v[98:101], v71 offset:17024
	ds_read_b128 v[102:105], v71 offset:25472
	ds_read_b128 v[106:109], v72 offset:128
	s_waitcnt lgkmcnt(5)
	v_mfma_f32_16x16x4_f32 v[74:77], v110, v126, v[74:77]
	v_mfma_f32_16x16x4_f32 v[78:81], v114, v126, v[78:81]
	v_mfma_f32_16x16x4_f32 v[82:85], v118, v126, v[82:85]
	v_mfma_f32_16x16x4_f32 v[86:89], v122, v126, v[86:89]
	v_mfma_f32_16x16x4_f32 v[74:77], v111, v127, v[74:77]
	v_mfma_f32_16x16x4_f32 v[78:81], v115, v127, v[78:81]
	v_mfma_f32_16x16x4_f32 v[82:85], v119, v127, v[82:85]
	v_mfma_f32_16x16x4_f32 v[86:89], v123, v127, v[86:89]
	v_mfma_f32_16x16x4_f32 v[74:77], v112, v128, v[74:77]
	v_mfma_f32_16x16x4_f32 v[78:81], v116, v128, v[78:81]
	v_mfma_f32_16x16x4_f32 v[82:85], v120, v128, v[82:85]
	v_mfma_f32_16x16x4_f32 v[86:89], v124, v128, v[86:89]
	v_mfma_f32_16x16x4_f32 v[74:77], v113, v129, v[74:77]
	v_mfma_f32_16x16x4_f32 v[78:81], v117, v129, v[78:81]
	v_mfma_f32_16x16x4_f32 v[82:85], v121, v129, v[82:85]
	v_mfma_f32_16x16x4_f32 v[86:89], v125, v129, v[86:89]
	ds_read_b128 v[110:113], v71 offset:192
	ds_read_b128 v[114:117], v71 offset:8640
	ds_read_b128 v[118:121], v71 offset:17088
	ds_read_b128 v[122:125], v71 offset:25536
	ds_read_b128 v[126:129], v72 offset:192
	s_waitcnt lgkmcnt(5)
	v_mfma_f32_16x16x4_f32 v[74:77], v90, v106, v[74:77]
	v_mfma_f32_16x16x4_f32 v[78:81], v94, v106, v[78:81]
	v_mfma_f32_16x16x4_f32 v[82:85], v98, v106, v[82:85]
	v_mfma_f32_16x16x4_f32 v[86:89], v102, v106, v[86:89]
	v_mfma_f32_16x16x4_f32 v[74:77], v91, v107, v[74:77]
	v_mfma_f32_16x16x4_f32 v[78:81], v95, v107, v[78:81]
	v_mfma_f32_16x16x4_f32 v[82:85], v99, v107, v[82:85]
	v_mfma_f32_16x16x4_f32 v[86:89], v103, v107, v[86:89]
	v_mfma_f32_16x16x4_f32 v[74:77], v92, v108, v[74:77]
	v_mfma_f32_16x16x4_f32 v[78:81], v96, v108, v[78:81]
	v_mfma_f32_16x16x4_f32 v[82:85], v100, v108, v[82:85]
	v_mfma_f32_16x16x4_f32 v[86:89], v104, v108, v[86:89]
	v_mfma_f32_16x16x4_f32 v[74:77], v93, v109, v[74:77]
	v_mfma_f32_16x16x4_f32 v[78:81], v97, v109, v[78:81]
	v_mfma_f32_16x16x4_f32 v[82:85], v101, v109, v[82:85]
	v_mfma_f32_16x16x4_f32 v[86:89], v105, v109, v[86:89]
	ds_read_b128 v[90:93], v71 offset:256
	ds_read_b128 v[94:97], v71 offset:8704
	ds_read_b128 v[98:101], v71 offset:17152
	ds_read_b128 v[102:105], v71 offset:25600
	ds_read_b128 v[106:109], v72 offset:256
	s_waitcnt lgkmcnt(5)
	v_mfma_f32_16x16x4_f32 v[74:77], v110, v126, v[74:77]
	v_mfma_f32_16x16x4_f32 v[78:81], v114, v126, v[78:81]
	v_mfma_f32_16x16x4_f32 v[82:85], v118, v126, v[82:85]
	v_mfma_f32_16x16x4_f32 v[86:89], v122, v126, v[86:89]
	v_mfma_f32_16x16x4_f32 v[74:77], v111, v127, v[74:77]
	v_mfma_f32_16x16x4_f32 v[78:81], v115, v127, v[78:81]
	v_mfma_f32_16x16x4_f32 v[82:85], v119, v127, v[82:85]
	v_mfma_f32_16x16x4_f32 v[86:89], v123, v127, v[86:89]
	v_mfma_f32_16x16x4_f32 v[74:77], v112, v128, v[74:77]
	v_mfma_f32_16x16x4_f32 v[78:81], v116, v128, v[78:81]
	v_mfma_f32_16x16x4_f32 v[82:85], v120, v128, v[82:85]
	v_mfma_f32_16x16x4_f32 v[86:89], v124, v128, v[86:89]
	v_mfma_f32_16x16x4_f32 v[74:77], v113, v129, v[74:77]
	v_mfma_f32_16x16x4_f32 v[78:81], v117, v129, v[78:81]
	v_mfma_f32_16x16x4_f32 v[82:85], v121, v129, v[82:85]
	v_mfma_f32_16x16x4_f32 v[86:89], v125, v129, v[86:89]
	ds_read_b128 v[110:113], v71 offset:320
	ds_read_b128 v[114:117], v71 offset:8768
	ds_read_b128 v[118:121], v71 offset:17216
	ds_read_b128 v[122:125], v71 offset:25664
	ds_read_b128 v[126:129], v72 offset:320
	s_waitcnt lgkmcnt(5)
	v_mfma_f32_16x16x4_f32 v[74:77], v90, v106, v[74:77]
	v_mfma_f32_16x16x4_f32 v[78:81], v94, v106, v[78:81]
	v_mfma_f32_16x16x4_f32 v[82:85], v98, v106, v[82:85]
	v_mfma_f32_16x16x4_f32 v[86:89], v102, v106, v[86:89]
	v_mfma_f32_16x16x4_f32 v[74:77], v91, v107, v[74:77]
	v_mfma_f32_16x16x4_f32 v[78:81], v95, v107, v[78:81]
	v_mfma_f32_16x16x4_f32 v[82:85], v99, v107, v[82:85]
	v_mfma_f32_16x16x4_f32 v[86:89], v103, v107, v[86:89]
	v_mfma_f32_16x16x4_f32 v[74:77], v92, v108, v[74:77]
	v_mfma_f32_16x16x4_f32 v[78:81], v96, v108, v[78:81]
	v_mfma_f32_16x16x4_f32 v[82:85], v100, v108, v[82:85]
	v_mfma_f32_16x16x4_f32 v[86:89], v104, v108, v[86:89]
	v_mfma_f32_16x16x4_f32 v[74:77], v93, v109, v[74:77]
	v_mfma_f32_16x16x4_f32 v[78:81], v97, v109, v[78:81]
	v_mfma_f32_16x16x4_f32 v[82:85], v101, v109, v[82:85]
	v_mfma_f32_16x16x4_f32 v[86:89], v105, v109, v[86:89]
	ds_read_b128 v[90:93], v71 offset:384
	ds_read_b128 v[94:97], v71 offset:8832
	ds_read_b128 v[98:101], v71 offset:17280
	ds_read_b128 v[102:105], v71 offset:25728
	ds_read_b128 v[106:109], v72 offset:384
	s_waitcnt lgkmcnt(5)
	v_mfma_f32_16x16x4_f32 v[74:77], v110, v126, v[74:77]
	v_mfma_f32_16x16x4_f32 v[78:81], v114, v126, v[78:81]
	v_mfma_f32_16x16x4_f32 v[82:85], v118, v126, v[82:85]
	v_mfma_f32_16x16x4_f32 v[86:89], v122, v126, v[86:89]
	v_mfma_f32_16x16x4_f32 v[74:77], v111, v127, v[74:77]
	v_mfma_f32_16x16x4_f32 v[78:81], v115, v127, v[78:81]
	v_mfma_f32_16x16x4_f32 v[82:85], v119, v127, v[82:85]
	v_mfma_f32_16x16x4_f32 v[86:89], v123, v127, v[86:89]
	v_mfma_f32_16x16x4_f32 v[74:77], v112, v128, v[74:77]
	v_mfma_f32_16x16x4_f32 v[78:81], v116, v128, v[78:81]
	v_mfma_f32_16x16x4_f32 v[82:85], v120, v128, v[82:85]
	v_mfma_f32_16x16x4_f32 v[86:89], v124, v128, v[86:89]
	v_mfma_f32_16x16x4_f32 v[74:77], v113, v129, v[74:77]
	v_mfma_f32_16x16x4_f32 v[78:81], v117, v129, v[78:81]
	v_mfma_f32_16x16x4_f32 v[82:85], v121, v129, v[82:85]
	v_mfma_f32_16x16x4_f32 v[86:89], v125, v129, v[86:89]
	ds_read_b128 v[110:113], v71 offset:448
	ds_read_b128 v[114:117], v71 offset:8896
	ds_read_b128 v[118:121], v71 offset:17344
	ds_read_b128 v[122:125], v71 offset:25792
	ds_read_b128 v[126:129], v72 offset:448
	s_waitcnt lgkmcnt(5)
	v_mfma_f32_16x16x4_f32 v[74:77], v90, v106, v[74:77]
	v_mfma_f32_16x16x4_f32 v[78:81], v94, v106, v[78:81]
	v_mfma_f32_16x16x4_f32 v[82:85], v98, v106, v[82:85]
	v_mfma_f32_16x16x4_f32 v[86:89], v102, v106, v[86:89]
	v_mfma_f32_16x16x4_f32 v[74:77], v91, v107, v[74:77]
	v_mfma_f32_16x16x4_f32 v[78:81], v95, v107, v[78:81]
	v_mfma_f32_16x16x4_f32 v[82:85], v99, v107, v[82:85]
	v_mfma_f32_16x16x4_f32 v[86:89], v103, v107, v[86:89]
	v_mfma_f32_16x16x4_f32 v[74:77], v92, v108, v[74:77]
	v_mfma_f32_16x16x4_f32 v[78:81], v96, v108, v[78:81]
	v_mfma_f32_16x16x4_f32 v[82:85], v100, v108, v[82:85]
	v_mfma_f32_16x16x4_f32 v[86:89], v104, v108, v[86:89]
	v_mfma_f32_16x16x4_f32 v[74:77], v93, v109, v[74:77]
	v_mfma_f32_16x16x4_f32 v[78:81], v97, v109, v[78:81]
	v_mfma_f32_16x16x4_f32 v[82:85], v101, v109, v[82:85]
	v_mfma_f32_16x16x4_f32 v[86:89], v105, v109, v[86:89]
	s_waitcnt lgkmcnt(0)
	v_mfma_f32_16x16x4_f32 v[74:77], v110, v126, v[74:77]
	v_mfma_f32_16x16x4_f32 v[78:81], v114, v126, v[78:81]
	v_mfma_f32_16x16x4_f32 v[82:85], v118, v126, v[82:85]
	v_mfma_f32_16x16x4_f32 v[86:89], v122, v126, v[86:89]
	v_mfma_f32_16x16x4_f32 v[74:77], v111, v127, v[74:77]
	v_mfma_f32_16x16x4_f32 v[78:81], v115, v127, v[78:81]
	v_mfma_f32_16x16x4_f32 v[82:85], v119, v127, v[82:85]
	v_mfma_f32_16x16x4_f32 v[86:89], v123, v127, v[86:89]
	v_mfma_f32_16x16x4_f32 v[74:77], v112, v128, v[74:77]
	v_mfma_f32_16x16x4_f32 v[78:81], v116, v128, v[78:81]
	v_mfma_f32_16x16x4_f32 v[82:85], v120, v128, v[82:85]
	v_mfma_f32_16x16x4_f32 v[86:89], v124, v128, v[86:89]
	v_mfma_f32_16x16x4_f32 v[74:77], v113, v129, v[74:77]
	v_mfma_f32_16x16x4_f32 v[78:81], v117, v129, v[78:81]
	v_mfma_f32_16x16x4_f32 v[82:85], v121, v129, v[82:85]
	v_mfma_f32_16x16x4_f32 v[86:89], v125, v129, v[86:89]
	s_nop 15
	s_nop 3
	s_barrier
	v_cvt_pk_bf16_f32 v90, v74, v75
	v_cvt_pk_bf16_f32 v91, v76, v77
	ds_write_b64 v73, v[90:91]
	v_cvt_pk_bf16_f32 v92, v78, v79
	v_cvt_pk_bf16_f32 v93, v80, v81
	ds_write_b64 v73, v[92:93] offset:32
	v_cvt_pk_bf16_f32 v94, v82, v83
	v_cvt_pk_bf16_f32 v95, v84, v85
	ds_write_b64 v73, v[94:95] offset:64
	v_cvt_pk_bf16_f32 v96, v86, v87
	v_cvt_pk_bf16_f32 v97, v88, v89
	ds_write_b64 v73, v[96:97] offset:96
	s_waitcnt lgkmcnt(0)
	s_barrier
	ds_read_b128 v[0:3], v65
	v_add_u32_e32 v4, s6, v54
	s_lshl_b32 s4, s2, 1
	v_ashrrev_i32_e32 v5, 31, v4
	v_lshl_add_u64 v[38:39], v[12:13], 0, s[4:5]
	v_lshlrev_b64 v[4:5], 13, v[4:5]
	v_lshl_add_u64 v[40:41], v[38:39], 0, v[4:5]
	ds_read_b128 v[4:7], v66
	s_waitcnt lgkmcnt(1)
	global_store_dwordx4 v[40:41], v[0:3], off
	s_add_i32 s1, s1, s46
	s_cmpk_lt_i32 s1, 0x400
	v_add_u32_e32 v0, s6, v15
	v_ashrrev_i32_e32 v1, 31, v0
	v_lshlrev_b64 v[0:1], 13, v[0:1]
	v_lshl_add_u64 v[0:1], v[38:39], 0, v[0:1]
	s_waitcnt lgkmcnt(0)
	global_store_dwordx4 v[0:1], v[4:7], off
	s_barrier
	s_cbranch_scc1 .LBB0_52
